# v042 + P0 modulation k-loop with 4-deep ring of weight-row loads (saddr loads, LDS reads pipelined)
# baseline (speedup 1.0000x reference)
; #define GAS __attribute__((address_space(1)))
; #define LAS __attribute__((address_space(3)))
; __device__ __forceinline__ float sigmoidf_(float x) { return __builtin_amdgcn_rcpf(1.0f + __expf(-x)); }
; __device__ __forceinline__ void p0_mod_task(Frame& F, int task) {
;     const int l = task / 96, n0 = (task % 96) * 128;
;     LAS float* sc = (LAS float*)F.lds;
;     LAS float* red = (LAS float*)(F.lds + 9 * 2048 * 4);
;     for (int i = F.tid; i < 9 * DM; i += 512) { const int r = i >> 11, k = i & 2047; const float v = r < 8 ? F.in[I_C][r * DM + k] : F.in[I_CCTX][k]; sc[i] = v * sigmoidf_(v); }
;     __syncthreads();
;     const float* W = F.in[I_ADAW] + (size_t)l * DM * 6 * DM + n0 + 2 * F.lane;
;     float acc[9][2];
; #pragma unroll
;     for (int r = 0; r < 9; ++r) { acc[r][0] = 0.f; acc[r][1] = 0.f; }
;     const int kbase = F.wave * 256;
; #pragma unroll 8
;     for (int kk = 0; kk < 256; ++kk) { const int k = kbase + kk; const f32x2 w = *(const GAS f32x2*)(W + (size_t)k * (6 * DM));
; #pragma unroll
;         for (int r = 0; r < 9; ++r) { const float s = sc[r * DM + k]; acc[r][0] += s * w.x; acc[r][1] += s * w.y; } }
.LBB0_22:
	s_or_b64 exec, exec, s[0:1]
	s_mul_hi_i32 s0, s42, 0x2aaaaaab
	s_lshr_b32 s1, s0, 31
	s_ashr_i32 s0, s0, 4
	s_add_i32 s43, s0, s1
	s_mul_i32 s0, s43, 0x60
	s_sub_i32 s0, s42, s0
	s_lshl_b32 s0, s0, 7
	s_ashr_i32 s1, s0, 31
	s_mul_i32 s7, s43, 0x6000000
	s_lshl_b64 s[14:15], s[0:1], 2
	s_mul_hi_i32 s6, s43, 0x6000000
	s_add_u32 s0, s7, s14
	s_addc_u32 s1, s6, s15
	v_mov_b32_e32 v10, 0
	v_lshl_add_u64 v[8:9], v[6:7], 0, s[0:1]
	s_mov_b32 s0, 0
	v_mov_b32_e32 v11, v10
	v_mov_b32_e32 v12, v10
	v_mov_b32_e32 v13, v10
	v_mov_b32_e32 v14, v10
	v_mov_b32_e32 v15, v10
	v_mov_b32_e32 v16, v10
	v_mov_b32_e32 v17, v10
	v_mov_b32_e32 v18, v10
	v_mov_b32_e32 v19, v10
	v_mov_b32_e32 v20, v10
	v_mov_b32_e32 v21, v10
	v_mov_b32_e32 v22, v10
	v_mov_b32_e32 v23, v10
	v_mov_b32_e32 v24, v10
	v_mov_b32_e32 v25, v10
	v_mov_b32_e32 v26, v10
	v_mov_b32_e32 v27, v10
	s_waitcnt lgkmcnt(0)
	s_barrier
	v_readfirstlane_b32 s100, v8
	v_readfirstlane_b32 s101, v9
	v_lshlrev_b32_e32 v156, 3, v132
	v_mov_b32_e32 v157, s18
	s_nop 3
	s_sub_u32 s100, s100, 0x54000
	s_subb_u32 s101, s101, 0
	s_mov_b64 s[6:7], s[100:101]
	s_mov_b32 s0, 0
	v_add_u32_e32 v158, 0x10000, v157
	global_load_dwordx2 v[104:105], v156, s[100:101]
	s_add_u32 s100, s100, 0xc000
	s_addc_u32 s101, s101, 0
	global_load_dwordx2 v[106:107], v156, s[100:101]
	s_add_u32 s100, s100, 0xc000
	s_addc_u32 s101, s101, 0
	global_load_dwordx2 v[108:109], v156, s[100:101]
	s_add_u32 s100, s100, 0xc000
	s_addc_u32 s101, s101, 0
	global_load_dwordx2 v[110:111], v156, s[100:101]
	s_add_u32 s100, s100, 0xc000
	s_addc_u32 s101, s101, 0
	global_load_dwordx2 v[112:113], v156, s[100:101]
	s_add_u32 s100, s100, 0xc000
	s_addc_u32 s101, s101, 0
	global_load_dwordx2 v[114:115], v156, s[100:101]
	s_add_u32 s100, s100, 0xc000
	s_addc_u32 s101, s101, 0
	global_load_dwordx2 v[116:117], v156, s[100:101]
	s_add_u32 s100, s100, 0xc000
	s_addc_u32 s101, s101, 0
	global_load_dwordx2 v[118:119], v156, s[100:101]
	s_add_u32 s100, s100, 0xc000
	s_addc_u32 s101, s101, 0
	global_load_dwordx2 v[160:161], v156, s[100:101]
	s_add_u32 s100, s100, 0xc000
	s_addc_u32 s101, s101, 0
	global_load_dwordx2 v[162:163], v156, s[100:101]
	s_add_u32 s100, s100, 0xc000
	s_addc_u32 s101, s101, 0
	global_load_dwordx2 v[164:165], v156, s[100:101]
	s_add_u32 s100, s100, 0xc000
	s_addc_u32 s101, s101, 0
	global_load_dwordx2 v[166:167], v156, s[100:101]
	s_add_u32 s100, s100, 0xc000
	s_addc_u32 s101, s101, 0
	global_load_dwordx2 v[168:169], v156, s[100:101]
	s_add_u32 s100, s100, 0xc000
	s_addc_u32 s101, s101, 0
	global_load_dwordx2 v[170:171], v156, s[100:101]
	s_add_u32 s100, s100, 0xc000
	s_addc_u32 s101, s101, 0
	global_load_dwordx2 v[172:173], v156, s[100:101]
	s_add_u32 s100, s100, 0xc000
	s_addc_u32 s101, s101, 0
	global_load_dwordx2 v[174:175], v156, s[100:101]
	s_add_u32 s100, s100, 0xc000
	s_addc_u32 s101, s101, 0
	global_load_dwordx2 v[176:177], v156, s[100:101]
	s_add_u32 s100, s100, 0xc000
	s_addc_u32 s101, s101, 0
	global_load_dwordx2 v[178:179], v156, s[100:101]
	s_add_u32 s100, s100, 0xc000
	s_addc_u32 s101, s101, 0
	global_load_dwordx2 v[180:181], v156, s[100:101]
	s_add_u32 s100, s100, 0xc000
	s_addc_u32 s101, s101, 0
	global_load_dwordx2 v[182:183], v156, s[100:101]
	s_add_u32 s100, s100, 0xc000
	s_addc_u32 s101, s101, 0
	global_load_dwordx2 v[184:185], v156, s[100:101]
	s_add_u32 s100, s100, 0xc000
	s_addc_u32 s101, s101, 0
	global_load_dwordx2 v[186:187], v156, s[100:101]
	s_add_u32 s100, s100, 0xc000
	s_addc_u32 s101, s101, 0
	global_load_dwordx2 v[188:189], v156, s[100:101]
	s_add_u32 s100, s100, 0xc000
	s_addc_u32 s101, s101, 0
	global_load_dwordx2 v[190:191], v156, s[100:101]
	s_add_u32 s100, s100, 0xc000
	s_addc_u32 s101, s101, 0
	global_load_dwordx2 v[192:193], v156, s[100:101]
	s_add_u32 s100, s100, 0xc000
	s_addc_u32 s101, s101, 0
	global_load_dwordx2 v[194:195], v156, s[100:101]
	s_add_u32 s100, s100, 0xc000
	s_addc_u32 s101, s101, 0
	global_load_dwordx2 v[196:197], v156, s[100:101]
	s_add_u32 s100, s100, 0xc000
	s_addc_u32 s101, s101, 0
	global_load_dwordx2 v[198:199], v156, s[100:101]
	s_add_u32 s100, s100, 0xc000
	s_addc_u32 s101, s101, 0
	global_load_dwordx2 v[200:201], v156, s[100:101]
	s_add_u32 s100, s100, 0xc000
	s_addc_u32 s101, s101, 0
	global_load_dwordx2 v[202:203], v156, s[100:101]
	s_add_u32 s100, s100, 0xc000
	s_addc_u32 s101, s101, 0
	global_load_dwordx2 v[204:205], v156, s[100:101]
	s_add_u32 s100, s100, 0xc000
	s_addc_u32 s101, s101, 0
	global_load_dwordx2 v[206:207], v156, s[100:101]
	s_add_u32 s100, s100, 0xc000
	s_addc_u32 s101, s101, 0
	ds_read_b128 v[32:35], v157
	ds_read_b128 v[40:43], v157 offset:8192
	ds_read_b128 v[48:51], v157 offset:16384
	ds_read_b128 v[56:59], v157 offset:24576
	ds_read_b128 v[64:67], v157 offset:32768
	ds_read_b128 v[72:75], v157 offset:40960
	ds_read_b128 v[80:83], v157 offset:49152
	ds_read_b128 v[88:91], v157 offset:57344
	ds_read_b128 v[96:99], v158
	ds_read_b128 v[36:39], v157 offset:16
	ds_read_b128 v[44:47], v157 offset:8208
	ds_read_b128 v[52:55], v157 offset:16400
	ds_read_b128 v[60:63], v157 offset:24592
	ds_read_b128 v[68:71], v157 offset:32784
	ds_read_b128 v[76:79], v157 offset:40976
	ds_read_b128 v[84:87], v157 offset:49168
	ds_read_b128 v[92:95], v157 offset:57360
	ds_read_b128 v[100:103], v158 offset:16
.Lmodk_loop:
	s_cmpk_lg_i32 s0, 7
	s_cbranch_scc1 .Lmodk_nl
	s_mov_b64 s[100:101], s[6:7]
	v_mov_b32_e32 v156, 0
; #define GAS __attribute__((address_space(1)))
; __device__ __forceinline__ void p0_mod_task(Frame& F, int task) {
;     ...
; #pragma unroll 8
;     for (int kk = 0; kk < 256; ++kk) { const int k = kbase + kk; const f32x2 w = *(const GAS f32x2*)(W + (size_t)k * (6 * DM));
; #pragma unroll
;         for (int r = 0; r < 9; ++r) { const float s = sc[r * DM + k]; acc[r][0] += s * w.x; acc[r][1] += s * w.y; } }
.Lmodk_nl:
	s_waitcnt vmcnt(24) lgkmcnt(9)
	v_pk_fma_f32 v[12:13], v[104:105], v[32:33], v[12:13] op_sel_hi:[1,0,1]
	v_pk_fma_f32 v[14:15], v[104:105], v[40:41], v[14:15] op_sel_hi:[1,0,1]
	v_pk_fma_f32 v[16:17], v[104:105], v[48:49], v[16:17] op_sel_hi:[1,0,1]
	v_pk_fma_f32 v[18:19], v[104:105], v[56:57], v[18:19] op_sel_hi:[1,0,1]
	v_pk_fma_f32 v[20:21], v[104:105], v[64:65], v[20:21] op_sel_hi:[1,0,1]
	v_pk_fma_f32 v[22:23], v[104:105], v[72:73], v[22:23] op_sel_hi:[1,0,1]
	v_pk_fma_f32 v[24:25], v[104:105], v[80:81], v[24:25] op_sel_hi:[1,0,1]
	v_pk_fma_f32 v[26:27], v[104:105], v[88:89], v[26:27] op_sel_hi:[1,0,1]
	v_pk_fma_f32 v[10:11], v[104:105], v[96:97], v[10:11] op_sel_hi:[1,0,1]
	v_pk_fma_f32 v[12:13], v[106:107], v[32:33], v[12:13] op_sel:[0,1,0]
	v_pk_fma_f32 v[14:15], v[106:107], v[40:41], v[14:15] op_sel:[0,1,0]
	v_pk_fma_f32 v[16:17], v[106:107], v[48:49], v[16:17] op_sel:[0,1,0]
	v_pk_fma_f32 v[18:19], v[106:107], v[56:57], v[18:19] op_sel:[0,1,0]
	v_pk_fma_f32 v[20:21], v[106:107], v[64:65], v[20:21] op_sel:[0,1,0]
	v_pk_fma_f32 v[22:23], v[106:107], v[72:73], v[22:23] op_sel:[0,1,0]
	v_pk_fma_f32 v[24:25], v[106:107], v[80:81], v[24:25] op_sel:[0,1,0]
	v_pk_fma_f32 v[26:27], v[106:107], v[88:89], v[26:27] op_sel:[0,1,0]
	v_pk_fma_f32 v[10:11], v[106:107], v[96:97], v[10:11] op_sel:[0,1,0]
	v_pk_fma_f32 v[12:13], v[108:109], v[34:35], v[12:13] op_sel_hi:[1,0,1]
	v_pk_fma_f32 v[14:15], v[108:109], v[42:43], v[14:15] op_sel_hi:[1,0,1]
	v_pk_fma_f32 v[16:17], v[108:109], v[50:51], v[16:17] op_sel_hi:[1,0,1]
	v_pk_fma_f32 v[18:19], v[108:109], v[58:59], v[18:19] op_sel_hi:[1,0,1]
	v_pk_fma_f32 v[20:21], v[108:109], v[66:67], v[20:21] op_sel_hi:[1,0,1]
	v_pk_fma_f32 v[22:23], v[108:109], v[74:75], v[22:23] op_sel_hi:[1,0,1]
	v_pk_fma_f32 v[24:25], v[108:109], v[82:83], v[24:25] op_sel_hi:[1,0,1]
	v_pk_fma_f32 v[26:27], v[108:109], v[90:91], v[26:27] op_sel_hi:[1,0,1]
	v_pk_fma_f32 v[10:11], v[108:109], v[98:99], v[10:11] op_sel_hi:[1,0,1]
	v_pk_fma_f32 v[12:13], v[110:111], v[34:35], v[12:13] op_sel:[0,1,0]
	v_pk_fma_f32 v[14:15], v[110:111], v[42:43], v[14:15] op_sel:[0,1,0]
	v_pk_fma_f32 v[16:17], v[110:111], v[50:51], v[16:17] op_sel:[0,1,0]
	v_pk_fma_f32 v[18:19], v[110:111], v[58:59], v[18:19] op_sel:[0,1,0]
	v_pk_fma_f32 v[20:21], v[110:111], v[66:67], v[20:21] op_sel:[0,1,0]
	v_pk_fma_f32 v[22:23], v[110:111], v[74:75], v[22:23] op_sel:[0,1,0]
	v_pk_fma_f32 v[24:25], v[110:111], v[82:83], v[24:25] op_sel:[0,1,0]
	v_pk_fma_f32 v[26:27], v[110:111], v[90:91], v[26:27] op_sel:[0,1,0]
	v_pk_fma_f32 v[10:11], v[110:111], v[98:99], v[10:11] op_sel:[0,1,0]
	v_add_u32_e32 v157, 32, v157
	v_add_u32_e32 v158, 32, v158
	ds_read_b128 v[32:35], v157
	ds_read_b128 v[40:43], v157 offset:8192
	ds_read_b128 v[48:51], v157 offset:16384
	ds_read_b128 v[56:59], v157 offset:24576
	ds_read_b128 v[64:67], v157 offset:32768
	ds_read_b128 v[72:75], v157 offset:40960
	ds_read_b128 v[80:83], v157 offset:49152
	ds_read_b128 v[88:91], v157 offset:57344
	ds_read_b128 v[96:99], v158
	s_waitcnt lgkmcnt(9)
	v_pk_fma_f32 v[12:13], v[112:113], v[36:37], v[12:13] op_sel_hi:[1,0,1]
	v_pk_fma_f32 v[14:15], v[112:113], v[44:45], v[14:15] op_sel_hi:[1,0,1]
	v_pk_fma_f32 v[16:17], v[112:113], v[52:53], v[16:17] op_sel_hi:[1,0,1]
	v_pk_fma_f32 v[18:19], v[112:113], v[60:61], v[18:19] op_sel_hi:[1,0,1]
	v_pk_fma_f32 v[20:21], v[112:113], v[68:69], v[20:21] op_sel_hi:[1,0,1]
	v_pk_fma_f32 v[22:23], v[112:113], v[76:77], v[22:23] op_sel_hi:[1,0,1]
	v_pk_fma_f32 v[24:25], v[112:113], v[84:85], v[24:25] op_sel_hi:[1,0,1]
	v_pk_fma_f32 v[26:27], v[112:113], v[92:93], v[26:27] op_sel_hi:[1,0,1]
	v_pk_fma_f32 v[10:11], v[112:113], v[100:101], v[10:11] op_sel_hi:[1,0,1]
	v_pk_fma_f32 v[12:13], v[114:115], v[36:37], v[12:13] op_sel:[0,1,0]
	v_pk_fma_f32 v[14:15], v[114:115], v[44:45], v[14:15] op_sel:[0,1,0]
	v_pk_fma_f32 v[16:17], v[114:115], v[52:53], v[16:17] op_sel:[0,1,0]
	v_pk_fma_f32 v[18:19], v[114:115], v[60:61], v[18:19] op_sel:[0,1,0]
	v_pk_fma_f32 v[20:21], v[114:115], v[68:69], v[20:21] op_sel:[0,1,0]
	v_pk_fma_f32 v[22:23], v[114:115], v[76:77], v[22:23] op_sel:[0,1,0]
	v_pk_fma_f32 v[24:25], v[114:115], v[84:85], v[24:25] op_sel:[0,1,0]
	v_pk_fma_f32 v[26:27], v[114:115], v[92:93], v[26:27] op_sel:[0,1,0]
	v_pk_fma_f32 v[10:11], v[114:115], v[100:101], v[10:11] op_sel:[0,1,0]
	v_pk_fma_f32 v[12:13], v[116:117], v[38:39], v[12:13] op_sel_hi:[1,0,1]
	v_pk_fma_f32 v[14:15], v[116:117], v[46:47], v[14:15] op_sel_hi:[1,0,1]
	v_pk_fma_f32 v[16:17], v[116:117], v[54:55], v[16:17] op_sel_hi:[1,0,1]
	v_pk_fma_f32 v[18:19], v[116:117], v[62:63], v[18:19] op_sel_hi:[1,0,1]
	v_pk_fma_f32 v[20:21], v[116:117], v[70:71], v[20:21] op_sel_hi:[1,0,1]
	v_pk_fma_f32 v[22:23], v[116:117], v[78:79], v[22:23] op_sel_hi:[1,0,1]
	v_pk_fma_f32 v[24:25], v[116:117], v[86:87], v[24:25] op_sel_hi:[1,0,1]
	v_pk_fma_f32 v[26:27], v[116:117], v[94:95], v[26:27] op_sel_hi:[1,0,1]
	v_pk_fma_f32 v[10:11], v[116:117], v[102:103], v[10:11] op_sel_hi:[1,0,1]
	v_pk_fma_f32 v[12:13], v[118:119], v[38:39], v[12:13] op_sel:[0,1,0]
	v_pk_fma_f32 v[14:15], v[118:119], v[46:47], v[14:15] op_sel:[0,1,0]
	v_pk_fma_f32 v[16:17], v[118:119], v[54:55], v[16:17] op_sel:[0,1,0]
	v_pk_fma_f32 v[18:19], v[118:119], v[62:63], v[18:19] op_sel:[0,1,0]
	v_pk_fma_f32 v[20:21], v[118:119], v[70:71], v[20:21] op_sel:[0,1,0]
	v_pk_fma_f32 v[22:23], v[118:119], v[78:79], v[22:23] op_sel:[0,1,0]
	v_pk_fma_f32 v[24:25], v[118:119], v[86:87], v[24:25] op_sel:[0,1,0]
	v_pk_fma_f32 v[26:27], v[118:119], v[94:95], v[26:27] op_sel:[0,1,0]
	v_pk_fma_f32 v[10:11], v[118:119], v[102:103], v[10:11] op_sel:[0,1,0]
	ds_read_b128 v[36:39], v157 offset:16
	ds_read_b128 v[44:47], v157 offset:8208
	ds_read_b128 v[52:55], v157 offset:16400
	ds_read_b128 v[60:63], v157 offset:24592
	ds_read_b128 v[68:71], v157 offset:32784
	ds_read_b128 v[76:79], v157 offset:40976
	ds_read_b128 v[84:87], v157 offset:49168
	ds_read_b128 v[92:95], v157 offset:57360
	ds_read_b128 v[100:103], v158 offset:16
	global_load_dwordx2 v[104:105], v156, s[100:101]
	s_add_u32 s100, s100, 0xc000
	s_addc_u32 s101, s101, 0
	global_load_dwordx2 v[106:107], v156, s[100:101]
	s_add_u32 s100, s100, 0xc000
	s_addc_u32 s101, s101, 0
	global_load_dwordx2 v[108:109], v156, s[100:101]
	s_add_u32 s100, s100, 0xc000
	s_addc_u32 s101, s101, 0
	global_load_dwordx2 v[110:111], v156, s[100:101]
	s_add_u32 s100, s100, 0xc000
	s_addc_u32 s101, s101, 0
	global_load_dwordx2 v[112:113], v156, s[100:101]
	s_add_u32 s100, s100, 0xc000
	s_addc_u32 s101, s101, 0
	global_load_dwordx2 v[114:115], v156, s[100:101]
	s_add_u32 s100, s100, 0xc000
	s_addc_u32 s101, s101, 0
	global_load_dwordx2 v[116:117], v156, s[100:101]
	s_add_u32 s100, s100, 0xc000
	s_addc_u32 s101, s101, 0
	global_load_dwordx2 v[118:119], v156, s[100:101]
	s_add_u32 s100, s100, 0xc000
	s_addc_u32 s101, s101, 0
	s_waitcnt vmcnt(24) lgkmcnt(9)
; #define GAS __attribute__((address_space(1)))
; __device__ __forceinline__ void p0_mod_task(Frame& F, int task) {
;     ...
; #pragma unroll 8
;     for (int kk = 0; kk < 256; ++kk) { const int k = kbase + kk; const f32x2 w = *(const GAS f32x2*)(W + (size_t)k * (6 * DM));
; #pragma unroll
;         for (int r = 0; r < 9; ++r) { const float s = sc[r * DM + k]; acc[r][0] += s * w.x; acc[r][1] += s * w.y; } }
	v_pk_fma_f32 v[12:13], v[160:161], v[32:33], v[12:13] op_sel_hi:[1,0,1]
	v_pk_fma_f32 v[14:15], v[160:161], v[40:41], v[14:15] op_sel_hi:[1,0,1]
	v_pk_fma_f32 v[16:17], v[160:161], v[48:49], v[16:17] op_sel_hi:[1,0,1]
	v_pk_fma_f32 v[18:19], v[160:161], v[56:57], v[18:19] op_sel_hi:[1,0,1]
	v_pk_fma_f32 v[20:21], v[160:161], v[64:65], v[20:21] op_sel_hi:[1,0,1]
	v_pk_fma_f32 v[22:23], v[160:161], v[72:73], v[22:23] op_sel_hi:[1,0,1]
	v_pk_fma_f32 v[24:25], v[160:161], v[80:81], v[24:25] op_sel_hi:[1,0,1]
	v_pk_fma_f32 v[26:27], v[160:161], v[88:89], v[26:27] op_sel_hi:[1,0,1]
	v_pk_fma_f32 v[10:11], v[160:161], v[96:97], v[10:11] op_sel_hi:[1,0,1]
	v_pk_fma_f32 v[12:13], v[162:163], v[32:33], v[12:13] op_sel:[0,1,0]
	v_pk_fma_f32 v[14:15], v[162:163], v[40:41], v[14:15] op_sel:[0,1,0]
	v_pk_fma_f32 v[16:17], v[162:163], v[48:49], v[16:17] op_sel:[0,1,0]
	v_pk_fma_f32 v[18:19], v[162:163], v[56:57], v[18:19] op_sel:[0,1,0]
	v_pk_fma_f32 v[20:21], v[162:163], v[64:65], v[20:21] op_sel:[0,1,0]
	v_pk_fma_f32 v[22:23], v[162:163], v[72:73], v[22:23] op_sel:[0,1,0]
	v_pk_fma_f32 v[24:25], v[162:163], v[80:81], v[24:25] op_sel:[0,1,0]
	v_pk_fma_f32 v[26:27], v[162:163], v[88:89], v[26:27] op_sel:[0,1,0]
	v_pk_fma_f32 v[10:11], v[162:163], v[96:97], v[10:11] op_sel:[0,1,0]
	v_pk_fma_f32 v[12:13], v[164:165], v[34:35], v[12:13] op_sel_hi:[1,0,1]
	v_pk_fma_f32 v[14:15], v[164:165], v[42:43], v[14:15] op_sel_hi:[1,0,1]
	v_pk_fma_f32 v[16:17], v[164:165], v[50:51], v[16:17] op_sel_hi:[1,0,1]
	v_pk_fma_f32 v[18:19], v[164:165], v[58:59], v[18:19] op_sel_hi:[1,0,1]
	v_pk_fma_f32 v[20:21], v[164:165], v[66:67], v[20:21] op_sel_hi:[1,0,1]
	v_pk_fma_f32 v[22:23], v[164:165], v[74:75], v[22:23] op_sel_hi:[1,0,1]
	v_pk_fma_f32 v[24:25], v[164:165], v[82:83], v[24:25] op_sel_hi:[1,0,1]
	v_pk_fma_f32 v[26:27], v[164:165], v[90:91], v[26:27] op_sel_hi:[1,0,1]
	v_pk_fma_f32 v[10:11], v[164:165], v[98:99], v[10:11] op_sel_hi:[1,0,1]
	v_pk_fma_f32 v[12:13], v[166:167], v[34:35], v[12:13] op_sel:[0,1,0]
	v_pk_fma_f32 v[14:15], v[166:167], v[42:43], v[14:15] op_sel:[0,1,0]
	v_pk_fma_f32 v[16:17], v[166:167], v[50:51], v[16:17] op_sel:[0,1,0]
	v_pk_fma_f32 v[18:19], v[166:167], v[58:59], v[18:19] op_sel:[0,1,0]
	v_pk_fma_f32 v[20:21], v[166:167], v[66:67], v[20:21] op_sel:[0,1,0]
	v_pk_fma_f32 v[22:23], v[166:167], v[74:75], v[22:23] op_sel:[0,1,0]
	v_pk_fma_f32 v[24:25], v[166:167], v[82:83], v[24:25] op_sel:[0,1,0]
	v_pk_fma_f32 v[26:27], v[166:167], v[90:91], v[26:27] op_sel:[0,1,0]
	v_pk_fma_f32 v[10:11], v[166:167], v[98:99], v[10:11] op_sel:[0,1,0]
	v_add_u32_e32 v157, 32, v157
	v_add_u32_e32 v158, 32, v158
	ds_read_b128 v[32:35], v157
	ds_read_b128 v[40:43], v157 offset:8192
	ds_read_b128 v[48:51], v157 offset:16384
	ds_read_b128 v[56:59], v157 offset:24576
	ds_read_b128 v[64:67], v157 offset:32768
	ds_read_b128 v[72:75], v157 offset:40960
	ds_read_b128 v[80:83], v157 offset:49152
	ds_read_b128 v[88:91], v157 offset:57344
	ds_read_b128 v[96:99], v158
	s_waitcnt lgkmcnt(9)
	v_pk_fma_f32 v[12:13], v[168:169], v[36:37], v[12:13] op_sel_hi:[1,0,1]
	v_pk_fma_f32 v[14:15], v[168:169], v[44:45], v[14:15] op_sel_hi:[1,0,1]
	v_pk_fma_f32 v[16:17], v[168:169], v[52:53], v[16:17] op_sel_hi:[1,0,1]
	v_pk_fma_f32 v[18:19], v[168:169], v[60:61], v[18:19] op_sel_hi:[1,0,1]
	v_pk_fma_f32 v[20:21], v[168:169], v[68:69], v[20:21] op_sel_hi:[1,0,1]
	v_pk_fma_f32 v[22:23], v[168:169], v[76:77], v[22:23] op_sel_hi:[1,0,1]
	v_pk_fma_f32 v[24:25], v[168:169], v[84:85], v[24:25] op_sel_hi:[1,0,1]
	v_pk_fma_f32 v[26:27], v[168:169], v[92:93], v[26:27] op_sel_hi:[1,0,1]
	v_pk_fma_f32 v[10:11], v[168:169], v[100:101], v[10:11] op_sel_hi:[1,0,1]
	v_pk_fma_f32 v[12:13], v[170:171], v[36:37], v[12:13] op_sel:[0,1,0]
	v_pk_fma_f32 v[14:15], v[170:171], v[44:45], v[14:15] op_sel:[0,1,0]
	v_pk_fma_f32 v[16:17], v[170:171], v[52:53], v[16:17] op_sel:[0,1,0]
	v_pk_fma_f32 v[18:19], v[170:171], v[60:61], v[18:19] op_sel:[0,1,0]
	v_pk_fma_f32 v[20:21], v[170:171], v[68:69], v[20:21] op_sel:[0,1,0]
	v_pk_fma_f32 v[22:23], v[170:171], v[76:77], v[22:23] op_sel:[0,1,0]
	v_pk_fma_f32 v[24:25], v[170:171], v[84:85], v[24:25] op_sel:[0,1,0]
	v_pk_fma_f32 v[26:27], v[170:171], v[92:93], v[26:27] op_sel:[0,1,0]
	v_pk_fma_f32 v[10:11], v[170:171], v[100:101], v[10:11] op_sel:[0,1,0]
	v_pk_fma_f32 v[12:13], v[172:173], v[38:39], v[12:13] op_sel_hi:[1,0,1]
	v_pk_fma_f32 v[14:15], v[172:173], v[46:47], v[14:15] op_sel_hi:[1,0,1]
	v_pk_fma_f32 v[16:17], v[172:173], v[54:55], v[16:17] op_sel_hi:[1,0,1]
	v_pk_fma_f32 v[18:19], v[172:173], v[62:63], v[18:19] op_sel_hi:[1,0,1]
	v_pk_fma_f32 v[20:21], v[172:173], v[70:71], v[20:21] op_sel_hi:[1,0,1]
	v_pk_fma_f32 v[22:23], v[172:173], v[78:79], v[22:23] op_sel_hi:[1,0,1]
	v_pk_fma_f32 v[24:25], v[172:173], v[86:87], v[24:25] op_sel_hi:[1,0,1]
	v_pk_fma_f32 v[26:27], v[172:173], v[94:95], v[26:27] op_sel_hi:[1,0,1]
	v_pk_fma_f32 v[10:11], v[172:173], v[102:103], v[10:11] op_sel_hi:[1,0,1]
	v_pk_fma_f32 v[12:13], v[174:175], v[38:39], v[12:13] op_sel:[0,1,0]
	v_pk_fma_f32 v[14:15], v[174:175], v[46:47], v[14:15] op_sel:[0,1,0]
	v_pk_fma_f32 v[16:17], v[174:175], v[54:55], v[16:17] op_sel:[0,1,0]
	v_pk_fma_f32 v[18:19], v[174:175], v[62:63], v[18:19] op_sel:[0,1,0]
	v_pk_fma_f32 v[20:21], v[174:175], v[70:71], v[20:21] op_sel:[0,1,0]
	v_pk_fma_f32 v[22:23], v[174:175], v[78:79], v[22:23] op_sel:[0,1,0]
	v_pk_fma_f32 v[24:25], v[174:175], v[86:87], v[24:25] op_sel:[0,1,0]
	v_pk_fma_f32 v[26:27], v[174:175], v[94:95], v[26:27] op_sel:[0,1,0]
	v_pk_fma_f32 v[10:11], v[174:175], v[102:103], v[10:11] op_sel:[0,1,0]
	ds_read_b128 v[36:39], v157 offset:16
	ds_read_b128 v[44:47], v157 offset:8208
	ds_read_b128 v[52:55], v157 offset:16400
	ds_read_b128 v[60:63], v157 offset:24592
	ds_read_b128 v[68:71], v157 offset:32784
	ds_read_b128 v[76:79], v157 offset:40976
	ds_read_b128 v[84:87], v157 offset:49168
	ds_read_b128 v[92:95], v157 offset:57360
	ds_read_b128 v[100:103], v158 offset:16
	global_load_dwordx2 v[160:161], v156, s[100:101]
	s_add_u32 s100, s100, 0xc000
	s_addc_u32 s101, s101, 0
	global_load_dwordx2 v[162:163], v156, s[100:101]
	s_add_u32 s100, s100, 0xc000
	s_addc_u32 s101, s101, 0
	global_load_dwordx2 v[164:165], v156, s[100:101]
	s_add_u32 s100, s100, 0xc000
	s_addc_u32 s101, s101, 0
	global_load_dwordx2 v[166:167], v156, s[100:101]
	s_add_u32 s100, s100, 0xc000
	s_addc_u32 s101, s101, 0
	global_load_dwordx2 v[168:169], v156, s[100:101]
	s_add_u32 s100, s100, 0xc000
	s_addc_u32 s101, s101, 0
	global_load_dwordx2 v[170:171], v156, s[100:101]
	s_add_u32 s100, s100, 0xc000
	s_addc_u32 s101, s101, 0
	global_load_dwordx2 v[172:173], v156, s[100:101]
	s_add_u32 s100, s100, 0xc000
	s_addc_u32 s101, s101, 0
	global_load_dwordx2 v[174:175], v156, s[100:101]
	s_add_u32 s100, s100, 0xc000
	s_addc_u32 s101, s101, 0
	s_waitcnt vmcnt(24) lgkmcnt(9)
; #define GAS __attribute__((address_space(1)))
; __device__ __forceinline__ void p0_mod_task(Frame& F, int task) {
;     ...
; #pragma unroll 8
;     for (int kk = 0; kk < 256; ++kk) { const int k = kbase + kk; const f32x2 w = *(const GAS f32x2*)(W + (size_t)k * (6 * DM));
; #pragma unroll
;         for (int r = 0; r < 9; ++r) { const float s = sc[r * DM + k]; acc[r][0] += s * w.x; acc[r][1] += s * w.y; } }
	v_pk_fma_f32 v[12:13], v[176:177], v[32:33], v[12:13] op_sel_hi:[1,0,1]
	v_pk_fma_f32 v[14:15], v[176:177], v[40:41], v[14:15] op_sel_hi:[1,0,1]
	v_pk_fma_f32 v[16:17], v[176:177], v[48:49], v[16:17] op_sel_hi:[1,0,1]
	v_pk_fma_f32 v[18:19], v[176:177], v[56:57], v[18:19] op_sel_hi:[1,0,1]
	v_pk_fma_f32 v[20:21], v[176:177], v[64:65], v[20:21] op_sel_hi:[1,0,1]
	v_pk_fma_f32 v[22:23], v[176:177], v[72:73], v[22:23] op_sel_hi:[1,0,1]
	v_pk_fma_f32 v[24:25], v[176:177], v[80:81], v[24:25] op_sel_hi:[1,0,1]
	v_pk_fma_f32 v[26:27], v[176:177], v[88:89], v[26:27] op_sel_hi:[1,0,1]
	v_pk_fma_f32 v[10:11], v[176:177], v[96:97], v[10:11] op_sel_hi:[1,0,1]
	v_pk_fma_f32 v[12:13], v[178:179], v[32:33], v[12:13] op_sel:[0,1,0]
	v_pk_fma_f32 v[14:15], v[178:179], v[40:41], v[14:15] op_sel:[0,1,0]
	v_pk_fma_f32 v[16:17], v[178:179], v[48:49], v[16:17] op_sel:[0,1,0]
	v_pk_fma_f32 v[18:19], v[178:179], v[56:57], v[18:19] op_sel:[0,1,0]
	v_pk_fma_f32 v[20:21], v[178:179], v[64:65], v[20:21] op_sel:[0,1,0]
	v_pk_fma_f32 v[22:23], v[178:179], v[72:73], v[22:23] op_sel:[0,1,0]
	v_pk_fma_f32 v[24:25], v[178:179], v[80:81], v[24:25] op_sel:[0,1,0]
	v_pk_fma_f32 v[26:27], v[178:179], v[88:89], v[26:27] op_sel:[0,1,0]
	v_pk_fma_f32 v[10:11], v[178:179], v[96:97], v[10:11] op_sel:[0,1,0]
	v_pk_fma_f32 v[12:13], v[180:181], v[34:35], v[12:13] op_sel_hi:[1,0,1]
	v_pk_fma_f32 v[14:15], v[180:181], v[42:43], v[14:15] op_sel_hi:[1,0,1]
	v_pk_fma_f32 v[16:17], v[180:181], v[50:51], v[16:17] op_sel_hi:[1,0,1]
	v_pk_fma_f32 v[18:19], v[180:181], v[58:59], v[18:19] op_sel_hi:[1,0,1]
	v_pk_fma_f32 v[20:21], v[180:181], v[66:67], v[20:21] op_sel_hi:[1,0,1]
	v_pk_fma_f32 v[22:23], v[180:181], v[74:75], v[22:23] op_sel_hi:[1,0,1]
	v_pk_fma_f32 v[24:25], v[180:181], v[82:83], v[24:25] op_sel_hi:[1,0,1]
	v_pk_fma_f32 v[26:27], v[180:181], v[90:91], v[26:27] op_sel_hi:[1,0,1]
	v_pk_fma_f32 v[10:11], v[180:181], v[98:99], v[10:11] op_sel_hi:[1,0,1]
	v_pk_fma_f32 v[12:13], v[182:183], v[34:35], v[12:13] op_sel:[0,1,0]
	v_pk_fma_f32 v[14:15], v[182:183], v[42:43], v[14:15] op_sel:[0,1,0]
	v_pk_fma_f32 v[16:17], v[182:183], v[50:51], v[16:17] op_sel:[0,1,0]
	v_pk_fma_f32 v[18:19], v[182:183], v[58:59], v[18:19] op_sel:[0,1,0]
	v_pk_fma_f32 v[20:21], v[182:183], v[66:67], v[20:21] op_sel:[0,1,0]
	v_pk_fma_f32 v[22:23], v[182:183], v[74:75], v[22:23] op_sel:[0,1,0]
	v_pk_fma_f32 v[24:25], v[182:183], v[82:83], v[24:25] op_sel:[0,1,0]
	v_pk_fma_f32 v[26:27], v[182:183], v[90:91], v[26:27] op_sel:[0,1,0]
	v_pk_fma_f32 v[10:11], v[182:183], v[98:99], v[10:11] op_sel:[0,1,0]
	v_add_u32_e32 v157, 32, v157
	v_add_u32_e32 v158, 32, v158
	ds_read_b128 v[32:35], v157
	ds_read_b128 v[40:43], v157 offset:8192
	ds_read_b128 v[48:51], v157 offset:16384
	ds_read_b128 v[56:59], v157 offset:24576
	ds_read_b128 v[64:67], v157 offset:32768
	ds_read_b128 v[72:75], v157 offset:40960
	ds_read_b128 v[80:83], v157 offset:49152
	ds_read_b128 v[88:91], v157 offset:57344
	ds_read_b128 v[96:99], v158
	s_waitcnt lgkmcnt(9)
	v_pk_fma_f32 v[12:13], v[184:185], v[36:37], v[12:13] op_sel_hi:[1,0,1]
	v_pk_fma_f32 v[14:15], v[184:185], v[44:45], v[14:15] op_sel_hi:[1,0,1]
	v_pk_fma_f32 v[16:17], v[184:185], v[52:53], v[16:17] op_sel_hi:[1,0,1]
	v_pk_fma_f32 v[18:19], v[184:185], v[60:61], v[18:19] op_sel_hi:[1,0,1]
	v_pk_fma_f32 v[20:21], v[184:185], v[68:69], v[20:21] op_sel_hi:[1,0,1]
	v_pk_fma_f32 v[22:23], v[184:185], v[76:77], v[22:23] op_sel_hi:[1,0,1]
	v_pk_fma_f32 v[24:25], v[184:185], v[84:85], v[24:25] op_sel_hi:[1,0,1]
	v_pk_fma_f32 v[26:27], v[184:185], v[92:93], v[26:27] op_sel_hi:[1,0,1]
	v_pk_fma_f32 v[10:11], v[184:185], v[100:101], v[10:11] op_sel_hi:[1,0,1]
	v_pk_fma_f32 v[12:13], v[186:187], v[36:37], v[12:13] op_sel:[0,1,0]
	v_pk_fma_f32 v[14:15], v[186:187], v[44:45], v[14:15] op_sel:[0,1,0]
	v_pk_fma_f32 v[16:17], v[186:187], v[52:53], v[16:17] op_sel:[0,1,0]
	v_pk_fma_f32 v[18:19], v[186:187], v[60:61], v[18:19] op_sel:[0,1,0]
	v_pk_fma_f32 v[20:21], v[186:187], v[68:69], v[20:21] op_sel:[0,1,0]
	v_pk_fma_f32 v[22:23], v[186:187], v[76:77], v[22:23] op_sel:[0,1,0]
	v_pk_fma_f32 v[24:25], v[186:187], v[84:85], v[24:25] op_sel:[0,1,0]
	v_pk_fma_f32 v[26:27], v[186:187], v[92:93], v[26:27] op_sel:[0,1,0]
	v_pk_fma_f32 v[10:11], v[186:187], v[100:101], v[10:11] op_sel:[0,1,0]
	v_pk_fma_f32 v[12:13], v[188:189], v[38:39], v[12:13] op_sel_hi:[1,0,1]
	v_pk_fma_f32 v[14:15], v[188:189], v[46:47], v[14:15] op_sel_hi:[1,0,1]
	v_pk_fma_f32 v[16:17], v[188:189], v[54:55], v[16:17] op_sel_hi:[1,0,1]
	v_pk_fma_f32 v[18:19], v[188:189], v[62:63], v[18:19] op_sel_hi:[1,0,1]
	v_pk_fma_f32 v[20:21], v[188:189], v[70:71], v[20:21] op_sel_hi:[1,0,1]
	v_pk_fma_f32 v[22:23], v[188:189], v[78:79], v[22:23] op_sel_hi:[1,0,1]
	v_pk_fma_f32 v[24:25], v[188:189], v[86:87], v[24:25] op_sel_hi:[1,0,1]
	v_pk_fma_f32 v[26:27], v[188:189], v[94:95], v[26:27] op_sel_hi:[1,0,1]
	v_pk_fma_f32 v[10:11], v[188:189], v[102:103], v[10:11] op_sel_hi:[1,0,1]
	v_pk_fma_f32 v[12:13], v[190:191], v[38:39], v[12:13] op_sel:[0,1,0]
	v_pk_fma_f32 v[14:15], v[190:191], v[46:47], v[14:15] op_sel:[0,1,0]
	v_pk_fma_f32 v[16:17], v[190:191], v[54:55], v[16:17] op_sel:[0,1,0]
	v_pk_fma_f32 v[18:19], v[190:191], v[62:63], v[18:19] op_sel:[0,1,0]
	v_pk_fma_f32 v[20:21], v[190:191], v[70:71], v[20:21] op_sel:[0,1,0]
	v_pk_fma_f32 v[22:23], v[190:191], v[78:79], v[22:23] op_sel:[0,1,0]
	v_pk_fma_f32 v[24:25], v[190:191], v[86:87], v[24:25] op_sel:[0,1,0]
	v_pk_fma_f32 v[26:27], v[190:191], v[94:95], v[26:27] op_sel:[0,1,0]
	v_pk_fma_f32 v[10:11], v[190:191], v[102:103], v[10:11] op_sel:[0,1,0]
	ds_read_b128 v[36:39], v157 offset:16
	ds_read_b128 v[44:47], v157 offset:8208
	ds_read_b128 v[52:55], v157 offset:16400
	ds_read_b128 v[60:63], v157 offset:24592
	ds_read_b128 v[68:71], v157 offset:32784
	ds_read_b128 v[76:79], v157 offset:40976
	ds_read_b128 v[84:87], v157 offset:49168
	ds_read_b128 v[92:95], v157 offset:57360
	ds_read_b128 v[100:103], v158 offset:16
	global_load_dwordx2 v[176:177], v156, s[100:101]
	s_add_u32 s100, s100, 0xc000
	s_addc_u32 s101, s101, 0
	global_load_dwordx2 v[178:179], v156, s[100:101]
	s_add_u32 s100, s100, 0xc000
	s_addc_u32 s101, s101, 0
	global_load_dwordx2 v[180:181], v156, s[100:101]
	s_add_u32 s100, s100, 0xc000
	s_addc_u32 s101, s101, 0
	global_load_dwordx2 v[182:183], v156, s[100:101]
	s_add_u32 s100, s100, 0xc000
	s_addc_u32 s101, s101, 0
	global_load_dwordx2 v[184:185], v156, s[100:101]
	s_add_u32 s100, s100, 0xc000
	s_addc_u32 s101, s101, 0
	global_load_dwordx2 v[186:187], v156, s[100:101]
	s_add_u32 s100, s100, 0xc000
	s_addc_u32 s101, s101, 0
	global_load_dwordx2 v[188:189], v156, s[100:101]
	s_add_u32 s100, s100, 0xc000
	s_addc_u32 s101, s101, 0
	global_load_dwordx2 v[190:191], v156, s[100:101]
	s_add_u32 s100, s100, 0xc000
	s_addc_u32 s101, s101, 0
	s_waitcnt vmcnt(24) lgkmcnt(9)
; #define GAS __attribute__((address_space(1)))
; __device__ __forceinline__ void p0_mod_task(Frame& F, int task) {
;     ...
; #pragma unroll 8
;     for (int kk = 0; kk < 256; ++kk) { const int k = kbase + kk; const f32x2 w = *(const GAS f32x2*)(W + (size_t)k * (6 * DM));
; #pragma unroll
;         for (int r = 0; r < 9; ++r) { const float s = sc[r * DM + k]; acc[r][0] += s * w.x; acc[r][1] += s * w.y; } }
	v_pk_fma_f32 v[12:13], v[192:193], v[32:33], v[12:13] op_sel_hi:[1,0,1]
	v_pk_fma_f32 v[14:15], v[192:193], v[40:41], v[14:15] op_sel_hi:[1,0,1]
	v_pk_fma_f32 v[16:17], v[192:193], v[48:49], v[16:17] op_sel_hi:[1,0,1]
	v_pk_fma_f32 v[18:19], v[192:193], v[56:57], v[18:19] op_sel_hi:[1,0,1]
	v_pk_fma_f32 v[20:21], v[192:193], v[64:65], v[20:21] op_sel_hi:[1,0,1]
	v_pk_fma_f32 v[22:23], v[192:193], v[72:73], v[22:23] op_sel_hi:[1,0,1]
	v_pk_fma_f32 v[24:25], v[192:193], v[80:81], v[24:25] op_sel_hi:[1,0,1]
	v_pk_fma_f32 v[26:27], v[192:193], v[88:89], v[26:27] op_sel_hi:[1,0,1]
	v_pk_fma_f32 v[10:11], v[192:193], v[96:97], v[10:11] op_sel_hi:[1,0,1]
	v_pk_fma_f32 v[12:13], v[194:195], v[32:33], v[12:13] op_sel:[0,1,0]
	v_pk_fma_f32 v[14:15], v[194:195], v[40:41], v[14:15] op_sel:[0,1,0]
	v_pk_fma_f32 v[16:17], v[194:195], v[48:49], v[16:17] op_sel:[0,1,0]
	v_pk_fma_f32 v[18:19], v[194:195], v[56:57], v[18:19] op_sel:[0,1,0]
	v_pk_fma_f32 v[20:21], v[194:195], v[64:65], v[20:21] op_sel:[0,1,0]
	v_pk_fma_f32 v[22:23], v[194:195], v[72:73], v[22:23] op_sel:[0,1,0]
	v_pk_fma_f32 v[24:25], v[194:195], v[80:81], v[24:25] op_sel:[0,1,0]
	v_pk_fma_f32 v[26:27], v[194:195], v[88:89], v[26:27] op_sel:[0,1,0]
	v_pk_fma_f32 v[10:11], v[194:195], v[96:97], v[10:11] op_sel:[0,1,0]
	v_pk_fma_f32 v[12:13], v[196:197], v[34:35], v[12:13] op_sel_hi:[1,0,1]
	v_pk_fma_f32 v[14:15], v[196:197], v[42:43], v[14:15] op_sel_hi:[1,0,1]
	v_pk_fma_f32 v[16:17], v[196:197], v[50:51], v[16:17] op_sel_hi:[1,0,1]
	v_pk_fma_f32 v[18:19], v[196:197], v[58:59], v[18:19] op_sel_hi:[1,0,1]
	v_pk_fma_f32 v[20:21], v[196:197], v[66:67], v[20:21] op_sel_hi:[1,0,1]
	v_pk_fma_f32 v[22:23], v[196:197], v[74:75], v[22:23] op_sel_hi:[1,0,1]
	v_pk_fma_f32 v[24:25], v[196:197], v[82:83], v[24:25] op_sel_hi:[1,0,1]
	v_pk_fma_f32 v[26:27], v[196:197], v[90:91], v[26:27] op_sel_hi:[1,0,1]
	v_pk_fma_f32 v[10:11], v[196:197], v[98:99], v[10:11] op_sel_hi:[1,0,1]
	v_pk_fma_f32 v[12:13], v[198:199], v[34:35], v[12:13] op_sel:[0,1,0]
	v_pk_fma_f32 v[14:15], v[198:199], v[42:43], v[14:15] op_sel:[0,1,0]
	v_pk_fma_f32 v[16:17], v[198:199], v[50:51], v[16:17] op_sel:[0,1,0]
	v_pk_fma_f32 v[18:19], v[198:199], v[58:59], v[18:19] op_sel:[0,1,0]
	v_pk_fma_f32 v[20:21], v[198:199], v[66:67], v[20:21] op_sel:[0,1,0]
	v_pk_fma_f32 v[22:23], v[198:199], v[74:75], v[22:23] op_sel:[0,1,0]
	v_pk_fma_f32 v[24:25], v[198:199], v[82:83], v[24:25] op_sel:[0,1,0]
	v_pk_fma_f32 v[26:27], v[198:199], v[90:91], v[26:27] op_sel:[0,1,0]
	v_pk_fma_f32 v[10:11], v[198:199], v[98:99], v[10:11] op_sel:[0,1,0]
	v_add_u32_e32 v157, 32, v157
	v_add_u32_e32 v158, 32, v158
	ds_read_b128 v[32:35], v157
	ds_read_b128 v[40:43], v157 offset:8192
	ds_read_b128 v[48:51], v157 offset:16384
	ds_read_b128 v[56:59], v157 offset:24576
	ds_read_b128 v[64:67], v157 offset:32768
	ds_read_b128 v[72:75], v157 offset:40960
	ds_read_b128 v[80:83], v157 offset:49152
	ds_read_b128 v[88:91], v157 offset:57344
	ds_read_b128 v[96:99], v158
	s_waitcnt lgkmcnt(9)
	v_pk_fma_f32 v[12:13], v[200:201], v[36:37], v[12:13] op_sel_hi:[1,0,1]
	v_pk_fma_f32 v[14:15], v[200:201], v[44:45], v[14:15] op_sel_hi:[1,0,1]
	v_pk_fma_f32 v[16:17], v[200:201], v[52:53], v[16:17] op_sel_hi:[1,0,1]
	v_pk_fma_f32 v[18:19], v[200:201], v[60:61], v[18:19] op_sel_hi:[1,0,1]
	v_pk_fma_f32 v[20:21], v[200:201], v[68:69], v[20:21] op_sel_hi:[1,0,1]
	v_pk_fma_f32 v[22:23], v[200:201], v[76:77], v[22:23] op_sel_hi:[1,0,1]
	v_pk_fma_f32 v[24:25], v[200:201], v[84:85], v[24:25] op_sel_hi:[1,0,1]
	v_pk_fma_f32 v[26:27], v[200:201], v[92:93], v[26:27] op_sel_hi:[1,0,1]
	v_pk_fma_f32 v[10:11], v[200:201], v[100:101], v[10:11] op_sel_hi:[1,0,1]
	v_pk_fma_f32 v[12:13], v[202:203], v[36:37], v[12:13] op_sel:[0,1,0]
	v_pk_fma_f32 v[14:15], v[202:203], v[44:45], v[14:15] op_sel:[0,1,0]
	v_pk_fma_f32 v[16:17], v[202:203], v[52:53], v[16:17] op_sel:[0,1,0]
	v_pk_fma_f32 v[18:19], v[202:203], v[60:61], v[18:19] op_sel:[0,1,0]
	v_pk_fma_f32 v[20:21], v[202:203], v[68:69], v[20:21] op_sel:[0,1,0]
	v_pk_fma_f32 v[22:23], v[202:203], v[76:77], v[22:23] op_sel:[0,1,0]
	v_pk_fma_f32 v[24:25], v[202:203], v[84:85], v[24:25] op_sel:[0,1,0]
	v_pk_fma_f32 v[26:27], v[202:203], v[92:93], v[26:27] op_sel:[0,1,0]
	v_pk_fma_f32 v[10:11], v[202:203], v[100:101], v[10:11] op_sel:[0,1,0]
	v_pk_fma_f32 v[12:13], v[204:205], v[38:39], v[12:13] op_sel_hi:[1,0,1]
	v_pk_fma_f32 v[14:15], v[204:205], v[46:47], v[14:15] op_sel_hi:[1,0,1]
	v_pk_fma_f32 v[16:17], v[204:205], v[54:55], v[16:17] op_sel_hi:[1,0,1]
	v_pk_fma_f32 v[18:19], v[204:205], v[62:63], v[18:19] op_sel_hi:[1,0,1]
	v_pk_fma_f32 v[20:21], v[204:205], v[70:71], v[20:21] op_sel_hi:[1,0,1]
	v_pk_fma_f32 v[22:23], v[204:205], v[78:79], v[22:23] op_sel_hi:[1,0,1]
	v_pk_fma_f32 v[24:25], v[204:205], v[86:87], v[24:25] op_sel_hi:[1,0,1]
	v_pk_fma_f32 v[26:27], v[204:205], v[94:95], v[26:27] op_sel_hi:[1,0,1]
	v_pk_fma_f32 v[10:11], v[204:205], v[102:103], v[10:11] op_sel_hi:[1,0,1]
	v_pk_fma_f32 v[12:13], v[206:207], v[38:39], v[12:13] op_sel:[0,1,0]
	v_pk_fma_f32 v[14:15], v[206:207], v[46:47], v[14:15] op_sel:[0,1,0]
	v_pk_fma_f32 v[16:17], v[206:207], v[54:55], v[16:17] op_sel:[0,1,0]
	v_pk_fma_f32 v[18:19], v[206:207], v[62:63], v[18:19] op_sel:[0,1,0]
	v_pk_fma_f32 v[20:21], v[206:207], v[70:71], v[20:21] op_sel:[0,1,0]
	v_pk_fma_f32 v[22:23], v[206:207], v[78:79], v[22:23] op_sel:[0,1,0]
	v_pk_fma_f32 v[24:25], v[206:207], v[86:87], v[24:25] op_sel:[0,1,0]
	v_pk_fma_f32 v[26:27], v[206:207], v[94:95], v[26:27] op_sel:[0,1,0]
	v_pk_fma_f32 v[10:11], v[206:207], v[102:103], v[10:11] op_sel:[0,1,0]
	ds_read_b128 v[36:39], v157 offset:16
	ds_read_b128 v[44:47], v157 offset:8208
	ds_read_b128 v[52:55], v157 offset:16400
	ds_read_b128 v[60:63], v157 offset:24592
	ds_read_b128 v[68:71], v157 offset:32784
	ds_read_b128 v[76:79], v157 offset:40976
	ds_read_b128 v[84:87], v157 offset:49168
	ds_read_b128 v[92:95], v157 offset:57360
	ds_read_b128 v[100:103], v158 offset:16
	global_load_dwordx2 v[192:193], v156, s[100:101]
	s_add_u32 s100, s100, 0xc000
	s_addc_u32 s101, s101, 0
	global_load_dwordx2 v[194:195], v156, s[100:101]
	s_add_u32 s100, s100, 0xc000
	s_addc_u32 s101, s101, 0
	global_load_dwordx2 v[196:197], v156, s[100:101]
	s_add_u32 s100, s100, 0xc000
	s_addc_u32 s101, s101, 0
	global_load_dwordx2 v[198:199], v156, s[100:101]
	s_add_u32 s100, s100, 0xc000
	s_addc_u32 s101, s101, 0
	global_load_dwordx2 v[200:201], v156, s[100:101]
	s_add_u32 s100, s100, 0xc000
	s_addc_u32 s101, s101, 0
	global_load_dwordx2 v[202:203], v156, s[100:101]
	s_add_u32 s100, s100, 0xc000
	s_addc_u32 s101, s101, 0
	global_load_dwordx2 v[204:205], v156, s[100:101]
	s_add_u32 s100, s100, 0xc000
	s_addc_u32 s101, s101, 0
	global_load_dwordx2 v[206:207], v156, s[100:101]
	s_add_u32 s100, s100, 0xc000
	s_addc_u32 s101, s101, 0
	s_add_i32 s0, s0, 1
	s_cmpk_lt_i32 s0, 8
	s_cbranch_scc1 .Lmodk_loop
; __device__ __forceinline__ void p0_mod_task(Frame& F, int task) {
;     ...
; #pragma unroll
;     for (int r = 0; r < 9; ++r) { red[(F.wave * 9 + r) * 128 + 2 * F.lane] = acc[r][0]; red[(F.wave * 9 + r) * 128 + 2 * F.lane + 1] = acc[r][1]; }
;     __syncthreads();
;     float* mod = WSP(float, WS_MOD) + (size_t)l * 9 * 6 * DM;
;     for (int i = F.tid; i < 9 * 128; i += 512) { const int r = i >> 7, n = i & 127; float s = F.in[I_ADAB][(size_t)l * 6 * DM + n0 + n];
; #pragma unroll
;         for (int w = 0; w < 8; ++w) s += red[(w * 9 + r) * 128 + n];
;         mod[(size_t)r * 6 * DM + n0 + n] = s; }
	s_waitcnt vmcnt(0) lgkmcnt(0)
	ds_write2st64_b64 v31, v[12:13], v[14:15] offset1:1
	ds_write2st64_b64 v31, v[16:17], v[18:19] offset0:2 offset1:3
	ds_write2st64_b64 v31, v[20:21], v[22:23] offset0:4 offset1:5
	ds_write2st64_b64 v31, v[24:25], v[26:27] offset0:6 offset1:7
	ds_write_b64 v31, v[10:11] offset:4096
	s_waitcnt lgkmcnt(0)
	s_barrier
	s_and_saveexec_b64 s[0:1], s[4:5]
	s_cbranch_execz .LBB0_18
	s_mul_i32 s7, s43, 0x6c000
	s_mul_hi_i32 s6, s43, 0x6c000
	s_add_u32 s7, s16, s7
	s_addc_u32 s44, s17, s6
	s_add_u32 s6, s7, s14
	s_addc_u32 s7, s44, s15
	s_mul_hi_i32 s44, s43, 0xc000
	s_mul_i32 s43, s43, 0xc000
	s_add_u32 s43, s2, s43
	s_addc_u32 s44, s3, s44
	s_add_u32 s14, s43, s14
	s_addc_u32 s15, s44, s15
	v_lshlrev_b32_e32 v4, 2, v28
	v_lshl_add_u64 v[8:9], s[14:15], 0, v[4:5]
	v_lshl_add_u64 v[10:11], s[6:7], 0, v[4:5]
	s_mov_b64 s[14:15], 0
	v_mov_b32_e32 v4, v0
